# sgu item epilogue (both layers): u and bias loads of the second 16-row half issued together with the first half's, one latency instead of two
# speedup vs baseline: 1.0024x; 1.0024x over previous
.LBB0_1006:
	ds_read_b64_tr_b16 v[82:83], v154
	ds_read_b64_tr_b16 v[86:87], v154 offset:32
	ds_read_b64_tr_b16 v[84:85], v145 offset:576
	ds_read_b64_tr_b16 v[88:89], v145 offset:608
	ds_read_b64_tr_b16 v[90:91], v154 offset:64
	ds_read_b64_tr_b16 v[92:93], v145 offset:640
	ds_read_b64_tr_b16 v[94:95], v154 offset:96
	ds_read_b64_tr_b16 v[96:97], v145 offset:672
	ds_read_b128 v[98:101], v155 offset:18432
	ds_read_b128 v[134:137], v155 offset:22784
	s_add_i32 s2, s22, s14
	s_ashr_i32 s3, s2, 31
	s_lshr_b32 s3, s3, 25
	s_waitcnt lgkmcnt(1)
	v_mfma_f32_16x16x32_bf16 v[102:105], v[82:85], v[98:101], 0
	s_add_i32 s3, s2, s3
	s_and_b32 s16, s3, 0xffffff80
	s_sub_i32 s14, s2, s16
	v_mfma_f32_16x16x32_bf16 v[106:109], v[86:89], v[98:101], 0
	s_ashr_i32 s15, s14, 31
	s_lshl_b64 s[14:15], s[14:15], 7
	s_ashr_i32 s17, s3, 7
	v_mfma_f32_16x16x32_bf16 v[110:113], v[90:93], v[98:101], 0
	s_lshl_b32 s18, s17, 6
	s_ashr_i32 s19, s18, 31
	v_mfma_f32_16x16x32_bf16 v[98:101], v[94:97], v[98:101], 0
	s_waitcnt lgkmcnt(0)
	v_mfma_f32_16x16x32_bf16 v[82:85], v[82:85], v[134:137], 0
	v_mfma_f32_16x16x32_bf16 v[86:89], v[86:89], v[134:137], 0
	v_mfma_f32_16x16x32_bf16 v[90:93], v[90:93], v[134:137], 0
	v_mfma_f32_16x16x32_bf16 v[94:97], v[94:97], v[134:137], 0
	ds_read_b64_tr_b16 v[134:135], v154 offset:4608
	ds_read_b64_tr_b16 v[136:137], v145 offset:5184
	ds_read_b64_tr_b16 v[138:139], v154 offset:4640
	ds_read_b64_tr_b16 v[140:141], v145 offset:5216
	ds_read_b64_tr_b16 v[160:161], v154 offset:4672
	ds_read_b64_tr_b16 v[162:163], v145 offset:5248
	ds_read_b64_tr_b16 v[164:165], v154 offset:4704
	ds_read_b64_tr_b16 v[166:167], v145 offset:5280
	ds_read_b128 v[168:171], v155 offset:18496
	s_waitcnt lgkmcnt(0)
	v_mfma_f32_16x16x32_bf16 v[102:105], v[134:137], v[168:171], v[102:105]
	v_mfma_f32_16x16x32_bf16 v[106:109], v[138:141], v[168:171], v[106:109]
	v_mfma_f32_16x16x32_bf16 v[110:113], v[160:163], v[168:171], v[110:113]
	v_mfma_f32_16x16x32_bf16 v[98:101], v[164:167], v[168:171], v[98:101]
	ds_read_b128 v[168:171], v155 offset:22848
	s_waitcnt lgkmcnt(0)
	v_mfma_f32_16x16x32_bf16 v[82:85], v[134:137], v[168:171], v[82:85]
	v_mfma_f32_16x16x32_bf16 v[86:89], v[138:141], v[168:171], v[86:89]
	v_mfma_f32_16x16x32_bf16 v[90:93], v[160:163], v[168:171], v[90:93]
	v_mfma_f32_16x16x32_bf16 v[94:97], v[164:167], v[168:171], v[94:97]
	ds_read_b64_tr_b16 v[134:135], v154 offset:9216
	ds_read_b64_tr_b16 v[136:137], v145 offset:9792
	ds_read_b64_tr_b16 v[138:139], v154 offset:9248
	ds_read_b64_tr_b16 v[140:141], v145 offset:9824
	ds_read_b64_tr_b16 v[160:161], v154 offset:9280
	ds_read_b64_tr_b16 v[162:163], v145 offset:9856
	ds_read_b64_tr_b16 v[164:165], v154 offset:9312
	ds_read_b64_tr_b16 v[166:167], v145 offset:9888
	ds_read_b128 v[168:171], v155 offset:18560
	s_waitcnt lgkmcnt(0)
	v_mfma_f32_16x16x32_bf16 v[172:175], v[160:163], v[168:171], v[110:113]
	s_nop 2
	ds_read_b128 v[110:113], v155 offset:22912
	v_mfma_f32_16x16x32_bf16 v[102:105], v[134:137], v[168:171], v[102:105]
	v_mfma_f32_16x16x32_bf16 v[106:109], v[138:141], v[168:171], v[106:109]
	v_mfma_f32_16x16x32_bf16 v[98:101], v[164:167], v[168:171], v[98:101]
	s_waitcnt lgkmcnt(0)
	v_mfma_f32_16x16x32_bf16 v[82:85], v[134:137], v[110:113], v[82:85]
	v_mfma_f32_16x16x32_bf16 v[86:89], v[138:141], v[110:113], v[86:89]
	v_mfma_f32_16x16x32_bf16 v[134:137], v[160:163], v[110:113], v[90:93]
	v_mfma_f32_16x16x32_bf16 v[138:141], v[164:167], v[110:113], v[94:97]
	s_nop 1
	ds_read_b64_tr_b16 v[90:91], v154 offset:13824
	ds_read_b64_tr_b16 v[92:93], v145 offset:14400
	ds_read_b64_tr_b16 v[160:161], v154 offset:13856
	ds_read_b64_tr_b16 v[162:163], v145 offset:14432
	ds_read_b64_tr_b16 v[164:165], v154 offset:13888
	ds_read_b64_tr_b16 v[166:167], v145 offset:14464
	ds_read_b64_tr_b16 v[168:169], v154 offset:13920
	ds_read_b64_tr_b16 v[170:171], v145 offset:14496
	ds_read_b128 v[94:97], v155 offset:18624
	s_waitcnt lgkmcnt(0)
	v_mfma_f32_16x16x32_bf16 v[110:113], v[90:93], v[94:97], v[102:105]
	v_mfma_f32_16x16x32_bf16 v[102:105], v[164:167], v[94:97], v[172:175]
	s_nop 2
	ds_read_b128 v[172:175], v155 offset:22976
	v_mfma_f32_16x16x32_bf16 v[106:109], v[160:163], v[94:97], v[106:109]
	v_mfma_f32_16x16x32_bf16 v[98:101], v[168:171], v[94:97], v[98:101]
	s_waitcnt lgkmcnt(0)
	v_mfma_f32_16x16x32_bf16 v[94:97], v[90:93], v[172:175], v[82:85]
	v_mfma_f32_16x16x32_bf16 v[90:93], v[160:163], v[172:175], v[86:89]
	v_mfma_f32_16x16x32_bf16 v[86:89], v[164:167], v[172:175], v[134:137]
	v_mfma_f32_16x16x32_bf16 v[82:85], v[168:171], v[172:175], v[138:141]
	s_nop 1
	v_mov_b64_e32 v[136:137], s[0:1]
	v_or_b32_e32 v134, s16, v116
	v_ashrrev_i32_e32 v135, 31, v134
	v_or_b32_e32 v138, s14, v116
	v_mad_u64_u32 v[136:137], s[20:21], v138, s25, v[136:137]
	v_mad_i32_i24 v137, s15, v157, v137
	v_lshl_add_u64 v[136:137], s[18:19], 1, v[136:137]
	v_lshl_add_u64 v[136:137], v[136:137], 0, v[114:115]
	v_add_co_u32_e32 v140, vcc, 0x1000, v136
	v_lshl_add_u64 v[134:135], v[134:135], 2, s[4:5]
	s_nop 0
	v_addc_co_u32_e32 v141, vcc, 0, v137, vcc
	v_add_co_u32_e32 v182, vcc, 0x34000, v140
	s_nop 1
	v_addc_co_u32_e32 v183, vcc, 0, v141, vcc
	global_load_dwordx2 v[176:177], v[140:141], off offset:4000
	global_load_dwordx2 v[178:179], v[140:141], off offset:4032
	global_load_dwordx2 v[180:181], v[140:141], off offset:4064
	global_load_dwordx2 v[140:141], v[140:141], off offset:3968
	v_mov_b32_e32 v139, s15
	global_load_dword v192, v[134:135], off offset:64
	global_load_dword v134, v[134:135], off
	global_load_dwordx2 v[184:185], v[182:183], off offset:4000
	global_load_dwordx2 v[186:187], v[182:183], off offset:4032
	global_load_dwordx2 v[188:189], v[182:183], off offset:4064
	global_load_dwordx2 v[190:191], v[182:183], off offset:3968
	s_waitcnt vmcnt(6)
	v_lshlrev_b32_e32 v123, 16, v140
	v_mul_f32_e32 v125, 0x3d372713, v123
	v_mul_f32_e32 v125, v125, v123
	v_fma_f32 v125, v125, v123, v123
	v_mul_f32_e32 v125, 0x3f4c422a, v125
	v_add_f32_e64 v127, |v125|, |v125|
	v_mul_f32_e32 v127, 0x3fb8aa3b, v127
	v_exp_f32_e32 v127, v127
	s_nop 0
	v_add_f32_e32 v127, 1.0, v127
	v_rcp_f32_e32 v127, v127
	s_nop 0
	v_fma_f32 v127, v127, -2.0, 1.0
	v_and_b32_e32 v129, 0xffff0000, v140
	v_mul_f32_e32 v131, 0x3d372713, v129
	v_mul_f32_e32 v131, v131, v129
	v_fma_f32 v131, v131, v129, v129
	v_mul_f32_e32 v131, 0x3f4c422a, v131
	v_add_f32_e64 v132, |v131|, |v131|
	v_mul_f32_e32 v132, 0x3fb8aa3b, v132
	v_exp_f32_e32 v132, v132
	s_nop 0
	v_add_f32_e32 v132, 1.0, v132
	v_rcp_f32_e32 v132, v132
	s_nop 0
	v_fma_f32 v132, v132, -2.0, 1.0
	v_lshlrev_b32_e32 v135, 16, v141
	v_mul_f32_e32 v140, 0x3d372713, v135
	v_mul_f32_e32 v140, v140, v135
	v_fma_f32 v140, v140, v135, v135
	v_mul_f32_e32 v140, 0x3f4c422a, v140
	v_add_f32_e64 v159, |v140|, |v140|
	v_mul_f32_e32 v159, 0x3fb8aa3b, v159
	v_exp_f32_e32 v159, v159
	s_nop 0
	v_add_f32_e32 v159, 1.0, v159
	v_rcp_f32_e32 v159, v159
	s_nop 0
	v_fma_f32 v159, v159, -2.0, 1.0
	v_and_b32_e32 v141, 0xffff0000, v141
	v_mul_f32_e32 v160, 0x3d372713, v141
	v_mul_f32_e32 v160, v160, v141
	v_fma_f32 v160, v160, v141, v141
	v_mul_f32_e32 v160, 0x3f4c422a, v160
	v_add_f32_e64 v161, |v160|, |v160|
	v_mul_f32_e32 v161, 0x3fb8aa3b, v161
	v_exp_f32_e32 v161, v161
	s_nop 0
	v_add_f32_e32 v161, 1.0, v161
	v_rcp_f32_e32 v161, v161
	s_nop 0
	v_fma_f32 v161, v161, -2.0, 1.0
	v_bfi_b32 v140, s30, v159, v140
	v_mul_f32_e32 v135, 0.5, v135
	v_add_f32_e32 v140, 1.0, v140
	v_mul_f32_e32 v135, v135, v140
	s_waitcnt vmcnt(4)
	v_add_f32_e32 v112, v112, v134
	v_mul_f32_e32 v140, v112, v135
	v_mul_f32_e32 v112, 0.5, v123
	v_bfi_b32 v123, s30, v127, v125
	v_add_f32_e32 v123, 1.0, v123
	v_mul_f32_e32 v112, v112, v123
	v_add_f32_e32 v110, v110, v134
	v_bfi_b32 v135, s30, v132, v131
	v_mov_b32_e32 v132, v111
	v_mul_f32_e32 v112, v110, v112
	v_mul_f32_e32 v123, 0.5, v129
	v_pk_add_f32 v[110:111], v[132:133], v[134:135]
	v_bfi_b32 v135, s30, v161, v160
	v_mul_f32_e32 v111, v123, v111
	v_mul_f32_e32 v110, v110, v111
	v_mov_b32_e32 v132, v113
	v_cvt_pk_bf16_f32 v112, v112, v110
	v_lshlrev_b64 v[110:111], 12, v[138:139]
	v_mul_f32_e32 v123, 0.5, v141
	v_pk_add_f32 v[138:139], v[132:133], v[134:135]
	v_lshl_add_u64 v[110:111], s[8:9], 0, v[110:111]
	v_mul_f32_e32 v113, v123, v139
	v_lshl_add_u64 v[110:111], s[18:19], 1, v[110:111]
	v_mul_f32_e32 v113, v138, v113
	v_lshl_add_u64 v[136:137], v[136:137], 0, s[10:11]
	v_lshl_add_u64 v[110:111], v[110:111], 0, v[114:115]
	v_cvt_pk_bf16_f32 v113, v140, v113
	global_store_dwordx2 v[110:111], v[112:113], off offset:2048
	v_mov_b64_e32 v[112:113], v[176:177]
	v_lshlrev_b32_e32 v123, 16, v112
	v_mul_f32_e32 v125, 0x3d372713, v123
	v_mul_f32_e32 v125, v125, v123
	v_fma_f32 v125, v125, v123, v123
	v_mul_f32_e32 v125, 0x3f4c422a, v125
	v_add_f32_e64 v127, |v125|, |v125|
	v_mul_f32_e32 v127, 0x3fb8aa3b, v127
	v_exp_f32_e32 v127, v127
	s_nop 0
	v_add_f32_e32 v127, 1.0, v127
	v_rcp_f32_e32 v127, v127
	s_nop 0
	v_fma_f32 v127, v127, -2.0, 1.0
	v_and_b32_e32 v112, 0xffff0000, v112
	v_mul_f32_e32 v129, 0x3d372713, v112
	v_mul_f32_e32 v129, v129, v112
	v_fma_f32 v129, v129, v112, v112
	v_mul_f32_e32 v129, 0x3f4c422a, v129
	v_add_f32_e64 v131, |v129|, |v129|
	v_mul_f32_e32 v131, 0x3fb8aa3b, v131
	v_exp_f32_e32 v131, v131
	s_nop 0
	v_add_f32_e32 v131, 1.0, v131
	v_rcp_f32_e32 v131, v131
	s_nop 0
	v_fma_f32 v131, v131, -2.0, 1.0
	v_lshlrev_b32_e32 v132, 16, v113
	v_mul_f32_e32 v135, 0x3d372713, v132
	v_mul_f32_e32 v135, v135, v132
	v_fma_f32 v135, v135, v132, v132
	v_mul_f32_e32 v135, 0x3f4c422a, v135
	v_add_f32_e64 v138, |v135|, |v135|
	v_mul_f32_e32 v138, 0x3fb8aa3b, v138
	v_exp_f32_e32 v138, v138
	s_nop 0
	v_add_f32_e32 v138, 1.0, v138
	v_rcp_f32_e32 v138, v138
	s_nop 0
	v_fma_f32 v138, v138, -2.0, 1.0
	v_and_b32_e32 v113, 0xffff0000, v113
	v_mul_f32_e32 v139, 0x3d372713, v113
	v_mul_f32_e32 v139, v139, v113
	v_fma_f32 v139, v139, v113, v113
	v_mul_f32_e32 v139, 0x3f4c422a, v139
	v_add_f32_e64 v140, |v139|, |v139|
	v_mul_f32_e32 v140, 0x3fb8aa3b, v140
	v_exp_f32_e32 v140, v140
	s_nop 0
	v_add_f32_e32 v140, 1.0, v140
	v_rcp_f32_e32 v140, v140
	s_nop 0
	v_fma_f32 v140, v140, -2.0, 1.0
	v_bfi_b32 v135, s30, v138, v135
	v_mul_f32_e32 v132, 0.5, v132
	v_add_f32_e32 v135, 1.0, v135
	v_mul_f32_e32 v132, v132, v135
	v_add_f32_e32 v108, v108, v134
	v_mul_f32_e32 v138, v108, v132
	v_mul_f32_e32 v108, 0.5, v123
	v_bfi_b32 v123, s30, v127, v125
	v_add_f32_e32 v123, 1.0, v123
	v_mul_f32_e32 v108, v108, v123
	v_add_f32_e32 v106, v106, v134
	v_bfi_b32 v135, s30, v131, v129
	v_mov_b32_e32 v132, v107
	v_mul_f32_e32 v108, v106, v108
	v_mul_f32_e32 v112, 0.5, v112
	v_pk_add_f32 v[106:107], v[132:133], v[134:135]
	v_bfi_b32 v135, s30, v140, v139
	v_mul_f32_e32 v107, v112, v107
	v_mul_f32_e32 v106, v106, v107
	v_mov_b32_e32 v132, v109
	v_cvt_pk_bf16_f32 v106, v108, v106
	v_mul_f32_e32 v107, 0.5, v113
	v_pk_add_f32 v[108:109], v[132:133], v[134:135]
	s_nop 0
	v_mul_f32_e32 v107, v107, v109
	v_mul_f32_e32 v107, v108, v107
	v_cvt_pk_bf16_f32 v107, v138, v107
	global_store_dwordx2 v[110:111], v[106:107], off offset:2080
	v_mov_b64_e32 v[106:107], v[178:179]
	v_lshlrev_b32_e32 v108, 16, v106
	v_mul_f32_e32 v109, 0x3d372713, v108
	v_mul_f32_e32 v109, v109, v108
	v_fma_f32 v109, v109, v108, v108
	v_mul_f32_e32 v109, 0x3f4c422a, v109
	v_add_f32_e64 v112, |v109|, |v109|
	v_mul_f32_e32 v112, 0x3fb8aa3b, v112
	v_exp_f32_e32 v112, v112
	s_nop 0
	v_add_f32_e32 v112, 1.0, v112
	v_rcp_f32_e32 v112, v112
	s_nop 0
	v_fma_f32 v112, v112, -2.0, 1.0
	v_and_b32_e32 v106, 0xffff0000, v106
	v_mul_f32_e32 v113, 0x3d372713, v106
	v_mul_f32_e32 v113, v113, v106
	v_fma_f32 v113, v113, v106, v106
	v_mul_f32_e32 v113, 0x3f4c422a, v113
	v_add_f32_e64 v123, |v113|, |v113|
	v_mul_f32_e32 v123, 0x3fb8aa3b, v123
	v_exp_f32_e32 v123, v123
	s_nop 0
	v_add_f32_e32 v123, 1.0, v123
	v_rcp_f32_e32 v123, v123
	s_nop 0
	v_fma_f32 v123, v123, -2.0, 1.0
	v_lshlrev_b32_e32 v125, 16, v107
	v_mul_f32_e32 v127, 0x3d372713, v125
	v_mul_f32_e32 v127, v127, v125
	v_fma_f32 v127, v127, v125, v125
	v_mul_f32_e32 v127, 0x3f4c422a, v127
	v_add_f32_e64 v129, |v127|, |v127|
	v_mul_f32_e32 v129, 0x3fb8aa3b, v129
	v_exp_f32_e32 v129, v129
	s_nop 0
	v_add_f32_e32 v129, 1.0, v129
	v_rcp_f32_e32 v129, v129
	s_nop 0
	v_fma_f32 v129, v129, -2.0, 1.0
	v_and_b32_e32 v107, 0xffff0000, v107
	v_mul_f32_e32 v131, 0x3d372713, v107
	v_mul_f32_e32 v131, v131, v107
	v_fma_f32 v131, v131, v107, v107
	v_mul_f32_e32 v131, 0x3f4c422a, v131
	v_add_f32_e64 v138, |v131|, |v131|
	v_mul_f32_e32 v138, 0x3fb8aa3b, v138
	v_exp_f32_e32 v138, v138
	s_nop 0
	v_add_f32_e32 v138, 1.0, v138
	v_rcp_f32_e32 v138, v138
	s_nop 0
	v_fma_f32 v138, v138, -2.0, 1.0
	v_bfi_b32 v127, s30, v129, v127
	v_mul_f32_e32 v125, 0.5, v125
	v_add_f32_e32 v127, 1.0, v127
	v_mul_f32_e32 v125, v125, v127
	v_add_f32_e32 v104, v104, v134
	v_mul_f32_e32 v125, v104, v125
	v_mul_f32_e32 v104, 0.5, v108
	v_bfi_b32 v108, s30, v112, v109
	v_add_f32_e32 v108, 1.0, v108
	v_mul_f32_e32 v104, v104, v108
	v_add_f32_e32 v102, v102, v134
	v_bfi_b32 v135, s30, v123, v113
	v_mov_b32_e32 v132, v103
	v_mul_f32_e32 v104, v102, v104
	v_mul_f32_e32 v106, 0.5, v106
	v_pk_add_f32 v[102:103], v[132:133], v[134:135]
	v_bfi_b32 v135, s30, v138, v131
	v_mul_f32_e32 v103, v106, v103
	v_mul_f32_e32 v102, v102, v103
	v_mov_b32_e32 v132, v105
	v_cvt_pk_bf16_f32 v102, v104, v102
	v_mul_f32_e32 v103, 0.5, v107
	v_pk_add_f32 v[104:105], v[132:133], v[134:135]
	s_nop 0
	v_mul_f32_e32 v103, v103, v105
	v_mul_f32_e32 v103, v104, v103
	v_cvt_pk_bf16_f32 v103, v125, v103
	global_store_dwordx2 v[110:111], v[102:103], off offset:2112
	v_mov_b64_e32 v[102:103], v[180:181]
	v_lshlrev_b32_e32 v104, 16, v102
	v_mul_f32_e32 v105, 0x3d372713, v104
	v_mul_f32_e32 v105, v105, v104
	v_fma_f32 v105, v105, v104, v104
	v_mul_f32_e32 v105, 0x3f4c422a, v105
	v_add_f32_e64 v106, |v105|, |v105|
	v_mul_f32_e32 v106, 0x3fb8aa3b, v106
	v_exp_f32_e32 v106, v106
	s_nop 0
	v_add_f32_e32 v106, 1.0, v106
	v_rcp_f32_e32 v106, v106
	s_nop 0
	v_fma_f32 v106, v106, -2.0, 1.0
	v_and_b32_e32 v102, 0xffff0000, v102
	v_mul_f32_e32 v107, 0x3d372713, v102
	v_mul_f32_e32 v107, v107, v102
	v_fma_f32 v107, v107, v102, v102
	v_mul_f32_e32 v107, 0x3f4c422a, v107
	v_add_f32_e64 v108, |v107|, |v107|
	v_mul_f32_e32 v108, 0x3fb8aa3b, v108
	v_exp_f32_e32 v108, v108
	s_nop 0
	v_add_f32_e32 v108, 1.0, v108
	v_rcp_f32_e32 v108, v108
	s_nop 0
	v_fma_f32 v108, v108, -2.0, 1.0
	v_lshlrev_b32_e32 v109, 16, v103
	v_mul_f32_e32 v112, 0x3d372713, v109
	v_mul_f32_e32 v112, v112, v109
	v_fma_f32 v112, v112, v109, v109
	v_mul_f32_e32 v112, 0x3f4c422a, v112
	v_add_f32_e64 v113, |v112|, |v112|
	v_mul_f32_e32 v113, 0x3fb8aa3b, v113
	v_exp_f32_e32 v113, v113
	s_nop 0
	v_add_f32_e32 v113, 1.0, v113
	v_rcp_f32_e32 v113, v113
	s_nop 0
	v_fma_f32 v113, v113, -2.0, 1.0
	v_and_b32_e32 v103, 0xffff0000, v103
	v_mul_f32_e32 v123, 0x3d372713, v103
	v_mul_f32_e32 v123, v123, v103
	v_fma_f32 v123, v123, v103, v103
	v_mul_f32_e32 v123, 0x3f4c422a, v123
	v_add_f32_e64 v125, |v123|, |v123|
	v_mul_f32_e32 v125, 0x3fb8aa3b, v125
	v_exp_f32_e32 v125, v125
	s_nop 0
	v_add_f32_e32 v125, 1.0, v125
	v_rcp_f32_e32 v125, v125
	s_nop 0
	v_fma_f32 v125, v125, -2.0, 1.0
	v_bfi_b32 v112, s30, v113, v112
	v_mul_f32_e32 v109, 0.5, v109
	v_add_f32_e32 v112, 1.0, v112
	v_mul_f32_e32 v109, v109, v112
	v_add_f32_e32 v100, v100, v134
	v_mul_f32_e32 v109, v100, v109
	v_mul_f32_e32 v100, 0.5, v104
	v_bfi_b32 v104, s30, v106, v105
	v_add_f32_e32 v104, 1.0, v104
	v_mul_f32_e32 v100, v100, v104
	v_add_f32_e32 v98, v98, v134
	v_bfi_b32 v135, s30, v108, v107
	v_mov_b32_e32 v132, v99
	v_mul_f32_e32 v100, v98, v100
	v_mul_f32_e32 v102, 0.5, v102
	v_pk_add_f32 v[98:99], v[132:133], v[134:135]
	v_bfi_b32 v135, s30, v125, v123
	v_mul_f32_e32 v99, v102, v99
	v_mul_f32_e32 v98, v98, v99
	v_mov_b32_e32 v132, v101
	v_cvt_pk_bf16_f32 v98, v100, v98
	v_mul_f32_e32 v99, 0.5, v103
	v_pk_add_f32 v[100:101], v[132:133], v[134:135]
	s_ashr_i32 s17, s16, 31
	v_mul_f32_e32 v99, v99, v101
	v_mul_f32_e32 v99, v100, v99
	v_cvt_pk_bf16_f32 v99, v109, v99
	v_or_b32_e32 v102, s14, v118
	v_mov_b64_e32 v[100:101], s[0:1]
	global_store_dwordx2 v[110:111], v[98:99], off offset:2144
	v_lshl_add_u64 v[98:99], s[16:17], 0, v[116:117]
	v_mad_u64_u32 v[100:101], s[16:17], v102, s25, v[100:101]
	v_mad_i32_i24 v101, s15, v157, v101
	v_lshl_add_u64 v[100:101], s[18:19], 1, v[100:101]
	v_lshl_add_u64 v[100:101], v[100:101], 0, v[114:115]
	v_add_co_u32_e32 v104, vcc, 0x1000, v100
	v_lshl_add_u64 v[98:99], v[98:99], 2, s[4:5]
	s_nop 0
	v_addc_co_u32_e32 v105, vcc, 0, v101, vcc
	s_waitcnt vmcnt(4)
	v_mov_b64 v[176:177], v[184:185]
	v_mov_b64 v[178:179], v[186:187]
	v_mov_b64 v[180:181], v[188:189]
	v_mov_b64 v[104:105], v[190:191]
	v_mov_b32_e32 v103, s15
	v_mov_b32_e32 v98, v192
	v_lshlrev_b32_e32 v99, 16, v104
	v_mul_f32_e32 v106, 0x3d372713, v99
	v_mul_f32_e32 v106, v106, v99
	v_fma_f32 v106, v106, v99, v99
	v_mul_f32_e32 v106, 0x3f4c422a, v106
	v_add_f32_e64 v107, |v106|, |v106|
	v_mul_f32_e32 v107, 0x3fb8aa3b, v107
	v_exp_f32_e32 v107, v107
	s_nop 0
	v_add_f32_e32 v107, 1.0, v107
	v_rcp_f32_e32 v107, v107
	s_nop 0
	v_fma_f32 v107, v107, -2.0, 1.0
	v_and_b32_e32 v104, 0xffff0000, v104
	v_mul_f32_e32 v108, 0x3d372713, v104
	v_mul_f32_e32 v108, v108, v104
	v_fma_f32 v108, v108, v104, v104
	v_mul_f32_e32 v108, 0x3f4c422a, v108
	v_add_f32_e64 v109, |v108|, |v108|
	v_mul_f32_e32 v109, 0x3fb8aa3b, v109
	v_exp_f32_e32 v109, v109
	s_nop 0
	v_add_f32_e32 v109, 1.0, v109
	v_rcp_f32_e32 v109, v109
	s_nop 0
	v_fma_f32 v109, v109, -2.0, 1.0
	v_lshlrev_b32_e32 v110, 16, v105
	v_mul_f32_e32 v111, 0x3d372713, v110
	v_mul_f32_e32 v111, v111, v110
	v_fma_f32 v111, v111, v110, v110
	v_mul_f32_e32 v111, 0x3f4c422a, v111
	v_add_f32_e64 v112, |v111|, |v111|
	v_mul_f32_e32 v112, 0x3fb8aa3b, v112
	v_exp_f32_e32 v112, v112
	s_nop 0
	v_add_f32_e32 v112, 1.0, v112
	v_rcp_f32_e32 v112, v112
	s_nop 0
	v_fma_f32 v112, v112, -2.0, 1.0
	v_and_b32_e32 v105, 0xffff0000, v105
	v_mul_f32_e32 v113, 0x3d372713, v105
	v_mul_f32_e32 v113, v113, v105
	v_fma_f32 v113, v113, v105, v105
	v_mul_f32_e32 v113, 0x3f4c422a, v113
	v_add_f32_e64 v123, |v113|, |v113|
	v_mul_f32_e32 v123, 0x3fb8aa3b, v123
	v_exp_f32_e32 v123, v123
	s_nop 0
	v_add_f32_e32 v123, 1.0, v123
	v_rcp_f32_e32 v123, v123
	s_nop 0
	v_fma_f32 v123, v123, -2.0, 1.0
	v_bfi_b32 v111, s30, v112, v111
	v_mul_f32_e32 v110, 0.5, v110
	v_add_f32_e32 v111, 1.0, v111
	v_mul_f32_e32 v110, v110, v111
	v_add_f32_e32 v96, v96, v98
	v_mul_f32_e32 v110, v96, v110
	v_mul_f32_e32 v96, 0.5, v99
	v_bfi_b32 v99, s30, v107, v106
	v_add_f32_e32 v99, 1.0, v99
	v_mul_f32_e32 v96, v96, v99
	v_add_f32_e32 v94, v94, v98
	v_bfi_b32 v99, s30, v109, v108
	v_mov_b32_e32 v132, v95
	v_mul_f32_e32 v96, v94, v96
	v_mul_f32_e32 v104, 0.5, v104
	v_pk_add_f32 v[94:95], v[132:133], v[98:99]
	v_bfi_b32 v99, s30, v123, v113
	v_mul_f32_e32 v95, v104, v95
	v_mul_f32_e32 v94, v94, v95
	v_mov_b32_e32 v132, v97
	v_cvt_pk_bf16_f32 v96, v96, v94
	v_lshlrev_b64 v[94:95], 12, v[102:103]
	v_mul_f32_e32 v104, 0.5, v105
	v_pk_add_f32 v[102:103], v[132:133], v[98:99]
	v_lshl_add_u64 v[94:95], s[8:9], 0, v[94:95]
	v_mul_f32_e32 v97, v104, v103
	v_lshl_add_u64 v[94:95], s[18:19], 1, v[94:95]
	v_mul_f32_e32 v97, v102, v97
	v_lshl_add_u64 v[100:101], v[100:101], 0, s[10:11]
	v_lshl_add_u64 v[94:95], v[94:95], 0, v[114:115]
	v_cvt_pk_bf16_f32 v97, v110, v97
	global_store_dwordx2 v[94:95], v[96:97], off offset:2048
	v_mov_b64_e32 v[96:97], v[176:177]
	v_lshlrev_b32_e32 v99, 16, v96
	v_mul_f32_e32 v102, 0x3d372713, v99
	v_mul_f32_e32 v102, v102, v99
	v_fma_f32 v102, v102, v99, v99
	v_mul_f32_e32 v102, 0x3f4c422a, v102
	v_add_f32_e64 v103, |v102|, |v102|
	v_mul_f32_e32 v103, 0x3fb8aa3b, v103
	v_exp_f32_e32 v103, v103
	s_nop 0
	v_add_f32_e32 v103, 1.0, v103
	v_rcp_f32_e32 v103, v103
	s_nop 0
	v_fma_f32 v103, v103, -2.0, 1.0
	v_and_b32_e32 v96, 0xffff0000, v96
	v_mul_f32_e32 v104, 0x3d372713, v96
	v_mul_f32_e32 v104, v104, v96
	v_fma_f32 v104, v104, v96, v96
	v_mul_f32_e32 v104, 0x3f4c422a, v104
	v_add_f32_e64 v105, |v104|, |v104|
	v_mul_f32_e32 v105, 0x3fb8aa3b, v105
	v_exp_f32_e32 v105, v105
	s_nop 0
	v_add_f32_e32 v105, 1.0, v105
	v_rcp_f32_e32 v105, v105
	s_nop 0
	v_fma_f32 v105, v105, -2.0, 1.0
	v_lshlrev_b32_e32 v106, 16, v97
	v_mul_f32_e32 v107, 0x3d372713, v106
	v_mul_f32_e32 v107, v107, v106
	v_fma_f32 v107, v107, v106, v106
	v_mul_f32_e32 v107, 0x3f4c422a, v107
	v_add_f32_e64 v108, |v107|, |v107|
	v_mul_f32_e32 v108, 0x3fb8aa3b, v108
	v_exp_f32_e32 v108, v108
	s_nop 0
	v_add_f32_e32 v108, 1.0, v108
	v_rcp_f32_e32 v108, v108
	s_nop 0
	v_fma_f32 v108, v108, -2.0, 1.0
	v_and_b32_e32 v97, 0xffff0000, v97
	v_mul_f32_e32 v109, 0x3d372713, v97
	v_mul_f32_e32 v109, v109, v97
	v_fma_f32 v109, v109, v97, v97
	v_mul_f32_e32 v109, 0x3f4c422a, v109
	v_add_f32_e64 v110, |v109|, |v109|
	v_mul_f32_e32 v110, 0x3fb8aa3b, v110
	v_exp_f32_e32 v110, v110
	s_nop 0
	v_add_f32_e32 v110, 1.0, v110
	v_rcp_f32_e32 v110, v110
	s_nop 0
	v_fma_f32 v110, v110, -2.0, 1.0
	v_bfi_b32 v107, s30, v108, v107
	v_mul_f32_e32 v106, 0.5, v106
	v_add_f32_e32 v107, 1.0, v107
	v_mul_f32_e32 v106, v106, v107
	v_add_f32_e32 v92, v92, v98
	v_mul_f32_e32 v106, v92, v106
	v_mul_f32_e32 v92, 0.5, v99
	v_bfi_b32 v99, s30, v103, v102
	v_add_f32_e32 v99, 1.0, v99
	v_mul_f32_e32 v92, v92, v99
	v_add_f32_e32 v90, v90, v98
	v_bfi_b32 v99, s30, v105, v104
	v_mov_b32_e32 v132, v91
	v_mul_f32_e32 v92, v90, v92
	v_mul_f32_e32 v96, 0.5, v96
	v_pk_add_f32 v[90:91], v[132:133], v[98:99]
	v_bfi_b32 v99, s30, v110, v109
	v_mul_f32_e32 v91, v96, v91
	v_mul_f32_e32 v90, v90, v91
	v_mov_b32_e32 v132, v93
	v_cvt_pk_bf16_f32 v90, v92, v90
	v_mul_f32_e32 v91, 0.5, v97
	v_pk_add_f32 v[92:93], v[132:133], v[98:99]
	s_nop 0
	v_mul_f32_e32 v91, v91, v93
	v_mul_f32_e32 v91, v92, v91
	v_cvt_pk_bf16_f32 v91, v106, v91
	global_store_dwordx2 v[94:95], v[90:91], off offset:2080
	v_mov_b64_e32 v[90:91], v[178:179]
	v_lshlrev_b32_e32 v92, 16, v90
	v_mul_f32_e32 v93, 0x3d372713, v92
	v_mul_f32_e32 v93, v93, v92
	v_fma_f32 v93, v93, v92, v92
	v_mul_f32_e32 v93, 0x3f4c422a, v93
	v_add_f32_e64 v96, |v93|, |v93|
	v_mul_f32_e32 v96, 0x3fb8aa3b, v96
	v_exp_f32_e32 v96, v96
	s_nop 0
	v_add_f32_e32 v96, 1.0, v96
	v_rcp_f32_e32 v96, v96
	s_nop 0
	v_fma_f32 v96, v96, -2.0, 1.0
	v_and_b32_e32 v90, 0xffff0000, v90
	v_mul_f32_e32 v97, 0x3d372713, v90
	v_mul_f32_e32 v97, v97, v90
	v_fma_f32 v97, v97, v90, v90
	v_mul_f32_e32 v97, 0x3f4c422a, v97
	v_add_f32_e64 v99, |v97|, |v97|
	v_mul_f32_e32 v99, 0x3fb8aa3b, v99
	v_exp_f32_e32 v99, v99
	s_nop 0
	v_add_f32_e32 v99, 1.0, v99
	v_rcp_f32_e32 v99, v99
	s_nop 0
	v_fma_f32 v99, v99, -2.0, 1.0
	v_lshlrev_b32_e32 v102, 16, v91
	v_mul_f32_e32 v103, 0x3d372713, v102
	v_mul_f32_e32 v103, v103, v102
	v_fma_f32 v103, v103, v102, v102
	v_mul_f32_e32 v103, 0x3f4c422a, v103
	v_add_f32_e64 v104, |v103|, |v103|
	v_mul_f32_e32 v104, 0x3fb8aa3b, v104
	v_exp_f32_e32 v104, v104
	s_nop 0
	v_add_f32_e32 v104, 1.0, v104
	v_rcp_f32_e32 v104, v104
	s_nop 0
	v_fma_f32 v104, v104, -2.0, 1.0
	v_and_b32_e32 v91, 0xffff0000, v91
	v_mul_f32_e32 v105, 0x3d372713, v91
	v_mul_f32_e32 v105, v105, v91
	v_fma_f32 v105, v105, v91, v91
	v_mul_f32_e32 v105, 0x3f4c422a, v105
	v_add_f32_e64 v106, |v105|, |v105|
	v_mul_f32_e32 v106, 0x3fb8aa3b, v106
	v_exp_f32_e32 v106, v106
	s_nop 0
	v_add_f32_e32 v106, 1.0, v106
	v_rcp_f32_e32 v106, v106
	s_nop 0
	v_fma_f32 v106, v106, -2.0, 1.0
	v_bfi_b32 v103, s30, v104, v103
	v_mul_f32_e32 v102, 0.5, v102
	v_add_f32_e32 v103, 1.0, v103
	v_mul_f32_e32 v102, v102, v103
	v_add_f32_e32 v88, v88, v98
	v_mul_f32_e32 v102, v88, v102
	v_mul_f32_e32 v88, 0.5, v92
	v_bfi_b32 v92, s30, v96, v93
	v_add_f32_e32 v92, 1.0, v92
	v_mul_f32_e32 v88, v88, v92
	v_add_f32_e32 v86, v86, v98
	v_bfi_b32 v99, s30, v99, v97
	v_mov_b32_e32 v132, v87
	v_mul_f32_e32 v88, v86, v88
	v_mul_f32_e32 v90, 0.5, v90
	v_pk_add_f32 v[86:87], v[132:133], v[98:99]
	v_bfi_b32 v99, s30, v106, v105
	v_mul_f32_e32 v87, v90, v87
	v_mul_f32_e32 v86, v86, v87
	v_mov_b32_e32 v132, v89
	v_cvt_pk_bf16_f32 v86, v88, v86
	v_mul_f32_e32 v87, 0.5, v91
	v_pk_add_f32 v[88:89], v[132:133], v[98:99]
	s_nop 0
	v_mul_f32_e32 v87, v87, v89
	v_mul_f32_e32 v87, v88, v87
	v_cvt_pk_bf16_f32 v87, v102, v87
	global_store_dwordx2 v[94:95], v[86:87], off offset:2112
	v_mov_b64_e32 v[86:87], v[180:181]
	v_lshlrev_b32_e32 v88, 16, v86
	v_mul_f32_e32 v89, 0x3d372713, v88
	v_mul_f32_e32 v89, v89, v88
	v_fma_f32 v89, v89, v88, v88
	v_mul_f32_e32 v89, 0x3f4c422a, v89
	v_add_f32_e64 v90, |v89|, |v89|
	v_mul_f32_e32 v90, 0x3fb8aa3b, v90
	v_exp_f32_e32 v90, v90
	s_nop 0
	v_add_f32_e32 v90, 1.0, v90
	v_rcp_f32_e32 v90, v90
	s_nop 0
	v_fma_f32 v90, v90, -2.0, 1.0
	v_and_b32_e32 v86, 0xffff0000, v86
	v_mul_f32_e32 v91, 0x3d372713, v86
	v_mul_f32_e32 v91, v91, v86
	v_fma_f32 v91, v91, v86, v86
	v_mul_f32_e32 v91, 0x3f4c422a, v91
	v_add_f32_e64 v92, |v91|, |v91|
	v_mul_f32_e32 v92, 0x3fb8aa3b, v92
	v_exp_f32_e32 v92, v92
	s_nop 0
	v_add_f32_e32 v92, 1.0, v92
	v_rcp_f32_e32 v92, v92
	s_nop 0
	v_fma_f32 v92, v92, -2.0, 1.0
	v_lshlrev_b32_e32 v93, 16, v87
	v_mul_f32_e32 v96, 0x3d372713, v93
	v_mul_f32_e32 v96, v96, v93
	v_fma_f32 v96, v96, v93, v93
	v_mul_f32_e32 v96, 0x3f4c422a, v96
	v_add_f32_e64 v97, |v96|, |v96|
	v_mul_f32_e32 v97, 0x3fb8aa3b, v97
	v_exp_f32_e32 v97, v97
	s_nop 0
	v_add_f32_e32 v97, 1.0, v97
	v_rcp_f32_e32 v97, v97
	s_nop 0
	v_fma_f32 v97, v97, -2.0, 1.0
	v_and_b32_e32 v87, 0xffff0000, v87
	v_mul_f32_e32 v99, 0x3d372713, v87
	v_mul_f32_e32 v99, v99, v87
	v_fma_f32 v99, v99, v87, v87
	v_mul_f32_e32 v100, 0x3f4c422a, v99
	v_cmp_nlt_f32_e64 s[14:15], |v100|, s26
	s_and_saveexec_b64 s[16:17], s[14:15]
	s_xor_b64 s[14:15], exec, s[16:17]
	s_cbranch_execz .LBB0_1132
	v_add_f32_e64 v99, |v100|, |v100|
	v_mul_f32_e32 v101, 0x3fb8aa3b, v99
	v_rndne_f32_e32 v102, v101
	v_sub_f32_e32 v103, v101, v102
	v_fma_f32 v101, v99, s27, -v101
	v_fmac_f32_e32 v101, 0x32a5705f, v99
	v_add_f32_e32 v101, v103, v101
	v_cvt_i32_f32_e32 v102, v102
	v_exp_f32_e32 v101, v101
	v_cmp_ngt_f32_e32 vcc, s28, v99
	v_ldexp_f32 v101, v101, v102
	s_nop 0
	v_cndmask_b32_e32 v101, 0, v101, vcc
	v_cmp_nlt_f32_e32 vcc, s29, v99
	s_nop 1
	v_cndmask_b32_e32 v99, v158, v101, vcc
	v_add_f32_e32 v99, 1.0, v99
	v_rcp_f32_e32 v99, v99
	s_nop 0
	v_fma_f32 v101, v99, -2.0, 1.0

.LBB0_3324:
	ds_read_b64_tr_b16 v[82:83], v154
	ds_read_b64_tr_b16 v[86:87], v154 offset:32
	ds_read_b64_tr_b16 v[84:85], v145 offset:576
	ds_read_b64_tr_b16 v[88:89], v145 offset:608
	ds_read_b64_tr_b16 v[90:91], v154 offset:64
	ds_read_b64_tr_b16 v[92:93], v145 offset:640
	ds_read_b64_tr_b16 v[94:95], v154 offset:96
	ds_read_b64_tr_b16 v[96:97], v145 offset:672
	ds_read_b128 v[98:101], v155 offset:18432
	ds_read_b128 v[134:137], v155 offset:22784
	s_add_i32 s2, s8, s18
	s_ashr_i32 s3, s2, 31
	s_lshr_b32 s3, s3, 25
	s_waitcnt lgkmcnt(1)
	v_mfma_f32_16x16x32_bf16 v[102:105], v[82:85], v[98:101], 0
	s_add_i32 s3, s2, s3
	s_and_b32 s20, s3, 0xffffff80
	s_sub_i32 s2, s2, s20
	v_mfma_f32_16x16x32_bf16 v[106:109], v[86:89], v[98:101], 0
	s_ashr_i32 s21, s3, 7
	s_ashr_i32 s3, s2, 31
	s_lshl_b64 s[18:19], s[2:3], 7
	v_mfma_f32_16x16x32_bf16 v[110:113], v[90:93], v[98:101], 0
	s_lshl_b32 s22, s21, 6
	s_ashr_i32 s23, s22, 31
	v_mfma_f32_16x16x32_bf16 v[98:101], v[94:97], v[98:101], 0
	s_waitcnt lgkmcnt(0)
	v_mfma_f32_16x16x32_bf16 v[82:85], v[82:85], v[134:137], 0
	v_mfma_f32_16x16x32_bf16 v[86:89], v[86:89], v[134:137], 0
	v_mfma_f32_16x16x32_bf16 v[90:93], v[90:93], v[134:137], 0
	v_mfma_f32_16x16x32_bf16 v[94:97], v[94:97], v[134:137], 0
	ds_read_b64_tr_b16 v[134:135], v154 offset:4608
	ds_read_b64_tr_b16 v[136:137], v145 offset:5184
	ds_read_b64_tr_b16 v[138:139], v154 offset:4640
	ds_read_b64_tr_b16 v[140:141], v145 offset:5216
	ds_read_b64_tr_b16 v[160:161], v154 offset:4672
	ds_read_b64_tr_b16 v[162:163], v145 offset:5248
	ds_read_b64_tr_b16 v[164:165], v154 offset:4704
	ds_read_b64_tr_b16 v[166:167], v145 offset:5280
	ds_read_b128 v[168:171], v155 offset:18496
	s_waitcnt lgkmcnt(0)
	v_mfma_f32_16x16x32_bf16 v[102:105], v[134:137], v[168:171], v[102:105]
	v_mfma_f32_16x16x32_bf16 v[106:109], v[138:141], v[168:171], v[106:109]
	v_mfma_f32_16x16x32_bf16 v[110:113], v[160:163], v[168:171], v[110:113]
	v_mfma_f32_16x16x32_bf16 v[98:101], v[164:167], v[168:171], v[98:101]
	ds_read_b128 v[168:171], v155 offset:22848
	s_waitcnt lgkmcnt(0)
	v_mfma_f32_16x16x32_bf16 v[82:85], v[134:137], v[168:171], v[82:85]
	v_mfma_f32_16x16x32_bf16 v[86:89], v[138:141], v[168:171], v[86:89]
	v_mfma_f32_16x16x32_bf16 v[90:93], v[160:163], v[168:171], v[90:93]
	v_mfma_f32_16x16x32_bf16 v[94:97], v[164:167], v[168:171], v[94:97]
	ds_read_b64_tr_b16 v[134:135], v154 offset:9216
	ds_read_b64_tr_b16 v[136:137], v145 offset:9792
	ds_read_b64_tr_b16 v[138:139], v154 offset:9248
	ds_read_b64_tr_b16 v[140:141], v145 offset:9824
	ds_read_b64_tr_b16 v[160:161], v154 offset:9280
	ds_read_b64_tr_b16 v[162:163], v145 offset:9856
	ds_read_b64_tr_b16 v[164:165], v154 offset:9312
	ds_read_b64_tr_b16 v[166:167], v145 offset:9888
	ds_read_b128 v[168:171], v155 offset:18560
	s_waitcnt lgkmcnt(0)
	v_mfma_f32_16x16x32_bf16 v[172:175], v[160:163], v[168:171], v[110:113]
	s_nop 2
	ds_read_b128 v[110:113], v155 offset:22912
	v_mfma_f32_16x16x32_bf16 v[102:105], v[134:137], v[168:171], v[102:105]
	v_mfma_f32_16x16x32_bf16 v[106:109], v[138:141], v[168:171], v[106:109]
	v_mfma_f32_16x16x32_bf16 v[98:101], v[164:167], v[168:171], v[98:101]
	s_waitcnt lgkmcnt(0)
	v_mfma_f32_16x16x32_bf16 v[82:85], v[134:137], v[110:113], v[82:85]
	v_mfma_f32_16x16x32_bf16 v[86:89], v[138:141], v[110:113], v[86:89]
	v_mfma_f32_16x16x32_bf16 v[134:137], v[160:163], v[110:113], v[90:93]
	v_mfma_f32_16x16x32_bf16 v[138:141], v[164:167], v[110:113], v[94:97]
	s_nop 1
	ds_read_b64_tr_b16 v[90:91], v154 offset:13824
	ds_read_b64_tr_b16 v[92:93], v145 offset:14400
	ds_read_b64_tr_b16 v[160:161], v154 offset:13856
	ds_read_b64_tr_b16 v[162:163], v145 offset:14432
	ds_read_b64_tr_b16 v[164:165], v154 offset:13888
	ds_read_b64_tr_b16 v[166:167], v145 offset:14464
	ds_read_b64_tr_b16 v[168:169], v154 offset:13920
	ds_read_b64_tr_b16 v[170:171], v145 offset:14496
	ds_read_b128 v[94:97], v155 offset:18624
	s_waitcnt lgkmcnt(0)
	v_mfma_f32_16x16x32_bf16 v[110:113], v[90:93], v[94:97], v[102:105]
	v_mfma_f32_16x16x32_bf16 v[102:105], v[164:167], v[94:97], v[172:175]
	s_nop 2
	ds_read_b128 v[172:175], v155 offset:22976
	v_mfma_f32_16x16x32_bf16 v[106:109], v[160:163], v[94:97], v[106:109]
	v_mfma_f32_16x16x32_bf16 v[98:101], v[168:171], v[94:97], v[98:101]
	s_waitcnt lgkmcnt(0)
	v_mfma_f32_16x16x32_bf16 v[94:97], v[90:93], v[172:175], v[82:85]
	v_mfma_f32_16x16x32_bf16 v[90:93], v[160:163], v[172:175], v[86:89]
	v_mfma_f32_16x16x32_bf16 v[86:89], v[164:167], v[172:175], v[134:137]
	v_mfma_f32_16x16x32_bf16 v[82:85], v[168:171], v[172:175], v[138:141]
	s_nop 1
	v_mov_b64_e32 v[136:137], s[0:1]
	v_or_b32_e32 v134, s20, v116
	v_ashrrev_i32_e32 v135, 31, v134
	v_or_b32_e32 v138, s18, v116
	v_mad_u64_u32 v[136:137], s[2:3], v138, s11, v[136:137]
	v_mad_i32_i24 v137, s19, v157, v137
	v_lshl_add_u64 v[136:137], s[22:23], 1, v[136:137]
	v_lshl_add_u64 v[136:137], v[136:137], 0, v[114:115]
	v_add_co_u32_e32 v140, vcc, 0x1000, v136
	v_lshl_add_u64 v[134:135], v[134:135], 2, s[6:7]
	s_nop 0
	v_addc_co_u32_e32 v141, vcc, 0, v137, vcc
	v_add_co_u32_e32 v182, vcc, 0x34000, v140
	s_nop 1
	v_addc_co_u32_e32 v183, vcc, 0, v141, vcc
	global_load_dwordx2 v[176:177], v[140:141], off offset:4000
	global_load_dwordx2 v[178:179], v[140:141], off offset:4032
	global_load_dwordx2 v[180:181], v[140:141], off offset:4064
	global_load_dwordx2 v[140:141], v[140:141], off offset:3968
	v_mov_b32_e32 v139, s19
	global_load_dword v192, v[134:135], off offset:64
	global_load_dword v134, v[134:135], off
	global_load_dwordx2 v[184:185], v[182:183], off offset:4000
	global_load_dwordx2 v[186:187], v[182:183], off offset:4032
	global_load_dwordx2 v[188:189], v[182:183], off offset:4064
	global_load_dwordx2 v[190:191], v[182:183], off offset:3968
	s_waitcnt vmcnt(6)
	v_lshlrev_b32_e32 v123, 16, v140
	v_mul_f32_e32 v125, 0x3d372713, v123
	v_mul_f32_e32 v125, v125, v123
	v_fma_f32 v125, v125, v123, v123
	v_mul_f32_e32 v125, 0x3f4c422a, v125
	v_add_f32_e64 v127, |v125|, |v125|
	v_mul_f32_e32 v127, 0x3fb8aa3b, v127
	v_exp_f32_e32 v127, v127
	s_nop 0
	v_add_f32_e32 v127, 1.0, v127
	v_rcp_f32_e32 v127, v127
	s_nop 0
	v_fma_f32 v127, v127, -2.0, 1.0
	v_and_b32_e32 v129, 0xffff0000, v140
	v_mul_f32_e32 v131, 0x3d372713, v129
	v_mul_f32_e32 v131, v131, v129
	v_fma_f32 v131, v131, v129, v129
	v_mul_f32_e32 v131, 0x3f4c422a, v131
	v_add_f32_e64 v132, |v131|, |v131|
	v_mul_f32_e32 v132, 0x3fb8aa3b, v132
	v_exp_f32_e32 v132, v132
	s_nop 0
	v_add_f32_e32 v132, 1.0, v132
	v_rcp_f32_e32 v132, v132
	s_nop 0
	v_fma_f32 v132, v132, -2.0, 1.0
	v_lshlrev_b32_e32 v135, 16, v141
	v_mul_f32_e32 v140, 0x3d372713, v135
	v_mul_f32_e32 v140, v140, v135
	v_fma_f32 v140, v140, v135, v135
	v_mul_f32_e32 v140, 0x3f4c422a, v140
	v_add_f32_e64 v159, |v140|, |v140|
	v_mul_f32_e32 v159, 0x3fb8aa3b, v159
	v_exp_f32_e32 v159, v159
	s_nop 0
	v_add_f32_e32 v159, 1.0, v159
	v_rcp_f32_e32 v159, v159
	s_nop 0
	v_fma_f32 v159, v159, -2.0, 1.0
	v_and_b32_e32 v141, 0xffff0000, v141
	v_mul_f32_e32 v160, 0x3d372713, v141
	v_mul_f32_e32 v160, v160, v141
	v_fma_f32 v160, v160, v141, v141
	v_mul_f32_e32 v160, 0x3f4c422a, v160
	v_add_f32_e64 v161, |v160|, |v160|
	v_mul_f32_e32 v161, 0x3fb8aa3b, v161
	v_exp_f32_e32 v161, v161
	s_nop 0
	v_add_f32_e32 v161, 1.0, v161
	v_rcp_f32_e32 v161, v161
	s_nop 0
	v_fma_f32 v161, v161, -2.0, 1.0
	v_bfi_b32 v140, s30, v159, v140
	v_mul_f32_e32 v135, 0.5, v135
	v_add_f32_e32 v140, 1.0, v140
	v_mul_f32_e32 v135, v135, v140
	s_waitcnt vmcnt(4)
	v_add_f32_e32 v112, v112, v134
	v_mul_f32_e32 v140, v112, v135
	v_mul_f32_e32 v112, 0.5, v123
	v_bfi_b32 v123, s30, v127, v125
	v_add_f32_e32 v123, 1.0, v123
	v_mul_f32_e32 v112, v112, v123
	v_add_f32_e32 v110, v110, v134
	v_bfi_b32 v135, s30, v132, v131
	v_mov_b32_e32 v132, v111
	v_mul_f32_e32 v112, v110, v112
	v_mul_f32_e32 v123, 0.5, v129
	v_pk_add_f32 v[110:111], v[132:133], v[134:135]
	v_bfi_b32 v135, s30, v161, v160
	v_mul_f32_e32 v111, v123, v111
	v_mul_f32_e32 v110, v110, v111
	v_mov_b32_e32 v132, v113
	v_cvt_pk_bf16_f32 v112, v112, v110
	v_lshlrev_b64 v[110:111], 12, v[138:139]
	v_mul_f32_e32 v123, 0.5, v141
	v_pk_add_f32 v[138:139], v[132:133], v[134:135]
	v_lshl_add_u64 v[110:111], s[12:13], 0, v[110:111]
	v_mul_f32_e32 v113, v123, v139
	v_lshl_add_u64 v[110:111], s[22:23], 1, v[110:111]
	v_mul_f32_e32 v113, v138, v113
	v_lshl_add_u64 v[136:137], v[136:137], 0, s[14:15]
	v_lshl_add_u64 v[110:111], v[110:111], 0, v[114:115]
	v_cvt_pk_bf16_f32 v113, v140, v113
	global_store_dwordx2 v[110:111], v[112:113], off offset:2048
	v_mov_b64_e32 v[112:113], v[176:177]
	v_lshlrev_b32_e32 v123, 16, v112
	v_mul_f32_e32 v125, 0x3d372713, v123
	v_mul_f32_e32 v125, v125, v123
	v_fma_f32 v125, v125, v123, v123
	v_mul_f32_e32 v125, 0x3f4c422a, v125
	v_add_f32_e64 v127, |v125|, |v125|
	v_mul_f32_e32 v127, 0x3fb8aa3b, v127
	v_exp_f32_e32 v127, v127
	s_nop 0
	v_add_f32_e32 v127, 1.0, v127
	v_rcp_f32_e32 v127, v127
	s_nop 0
	v_fma_f32 v127, v127, -2.0, 1.0
	v_and_b32_e32 v112, 0xffff0000, v112
	v_mul_f32_e32 v129, 0x3d372713, v112
	v_mul_f32_e32 v129, v129, v112
	v_fma_f32 v129, v129, v112, v112
	v_mul_f32_e32 v129, 0x3f4c422a, v129
	v_add_f32_e64 v131, |v129|, |v129|
	v_mul_f32_e32 v131, 0x3fb8aa3b, v131
	v_exp_f32_e32 v131, v131
	s_nop 0
	v_add_f32_e32 v131, 1.0, v131
	v_rcp_f32_e32 v131, v131
	s_nop 0
	v_fma_f32 v131, v131, -2.0, 1.0
	v_lshlrev_b32_e32 v132, 16, v113
	v_mul_f32_e32 v135, 0x3d372713, v132
	v_mul_f32_e32 v135, v135, v132
	v_fma_f32 v135, v135, v132, v132
	v_mul_f32_e32 v135, 0x3f4c422a, v135
	v_add_f32_e64 v138, |v135|, |v135|
	v_mul_f32_e32 v138, 0x3fb8aa3b, v138
	v_exp_f32_e32 v138, v138
	s_nop 0
	v_add_f32_e32 v138, 1.0, v138
	v_rcp_f32_e32 v138, v138
	s_nop 0
	v_fma_f32 v138, v138, -2.0, 1.0
	v_and_b32_e32 v113, 0xffff0000, v113
	v_mul_f32_e32 v139, 0x3d372713, v113
	v_mul_f32_e32 v139, v139, v113
	v_fma_f32 v139, v139, v113, v113
	v_mul_f32_e32 v139, 0x3f4c422a, v139
	v_add_f32_e64 v140, |v139|, |v139|
	v_mul_f32_e32 v140, 0x3fb8aa3b, v140
	v_exp_f32_e32 v140, v140
	s_nop 0
	v_add_f32_e32 v140, 1.0, v140
	v_rcp_f32_e32 v140, v140
	s_nop 0
	v_fma_f32 v140, v140, -2.0, 1.0
	v_bfi_b32 v135, s30, v138, v135
	v_mul_f32_e32 v132, 0.5, v132
	v_add_f32_e32 v135, 1.0, v135
	v_mul_f32_e32 v132, v132, v135
	v_add_f32_e32 v108, v108, v134
	v_mul_f32_e32 v138, v108, v132
	v_mul_f32_e32 v108, 0.5, v123
	v_bfi_b32 v123, s30, v127, v125
	v_add_f32_e32 v123, 1.0, v123
	v_mul_f32_e32 v108, v108, v123
	v_add_f32_e32 v106, v106, v134
	v_bfi_b32 v135, s30, v131, v129
	v_mov_b32_e32 v132, v107
	v_mul_f32_e32 v108, v106, v108
	v_mul_f32_e32 v112, 0.5, v112
	v_pk_add_f32 v[106:107], v[132:133], v[134:135]
	v_bfi_b32 v135, s30, v140, v139
	v_mul_f32_e32 v107, v112, v107
	v_mul_f32_e32 v106, v106, v107
	v_mov_b32_e32 v132, v109
	v_cvt_pk_bf16_f32 v106, v108, v106
	v_mul_f32_e32 v107, 0.5, v113
	v_pk_add_f32 v[108:109], v[132:133], v[134:135]
	s_nop 0
	v_mul_f32_e32 v107, v107, v109
	v_mul_f32_e32 v107, v108, v107
	v_cvt_pk_bf16_f32 v107, v138, v107
	global_store_dwordx2 v[110:111], v[106:107], off offset:2080
	v_mov_b64_e32 v[106:107], v[178:179]
	v_lshlrev_b32_e32 v108, 16, v106
	v_mul_f32_e32 v109, 0x3d372713, v108
	v_mul_f32_e32 v109, v109, v108
	v_fma_f32 v109, v109, v108, v108
	v_mul_f32_e32 v109, 0x3f4c422a, v109
	v_add_f32_e64 v112, |v109|, |v109|
	v_mul_f32_e32 v112, 0x3fb8aa3b, v112
	v_exp_f32_e32 v112, v112
	s_nop 0
	v_add_f32_e32 v112, 1.0, v112
	v_rcp_f32_e32 v112, v112
	s_nop 0
	v_fma_f32 v112, v112, -2.0, 1.0
	v_and_b32_e32 v106, 0xffff0000, v106
	v_mul_f32_e32 v113, 0x3d372713, v106
	v_mul_f32_e32 v113, v113, v106
	v_fma_f32 v113, v113, v106, v106
	v_mul_f32_e32 v113, 0x3f4c422a, v113
	v_add_f32_e64 v123, |v113|, |v113|
	v_mul_f32_e32 v123, 0x3fb8aa3b, v123
	v_exp_f32_e32 v123, v123
	s_nop 0
	v_add_f32_e32 v123, 1.0, v123
	v_rcp_f32_e32 v123, v123
	s_nop 0
	v_fma_f32 v123, v123, -2.0, 1.0
	v_lshlrev_b32_e32 v125, 16, v107
	v_mul_f32_e32 v127, 0x3d372713, v125
	v_mul_f32_e32 v127, v127, v125
	v_fma_f32 v127, v127, v125, v125
	v_mul_f32_e32 v127, 0x3f4c422a, v127
	v_add_f32_e64 v129, |v127|, |v127|
	v_mul_f32_e32 v129, 0x3fb8aa3b, v129
	v_exp_f32_e32 v129, v129
	s_nop 0
	v_add_f32_e32 v129, 1.0, v129
	v_rcp_f32_e32 v129, v129
	s_nop 0
	v_fma_f32 v129, v129, -2.0, 1.0
	v_and_b32_e32 v107, 0xffff0000, v107
	v_mul_f32_e32 v131, 0x3d372713, v107
	v_mul_f32_e32 v131, v131, v107
	v_fma_f32 v131, v131, v107, v107
	v_mul_f32_e32 v131, 0x3f4c422a, v131
	v_add_f32_e64 v138, |v131|, |v131|
	v_mul_f32_e32 v138, 0x3fb8aa3b, v138
	v_exp_f32_e32 v138, v138
	s_nop 0
	v_add_f32_e32 v138, 1.0, v138
	v_rcp_f32_e32 v138, v138
	s_nop 0
	v_fma_f32 v138, v138, -2.0, 1.0
	v_bfi_b32 v127, s30, v129, v127
	v_mul_f32_e32 v125, 0.5, v125
	v_add_f32_e32 v127, 1.0, v127
	v_mul_f32_e32 v125, v125, v127
	v_add_f32_e32 v104, v104, v134
	v_mul_f32_e32 v125, v104, v125
	v_mul_f32_e32 v104, 0.5, v108
	v_bfi_b32 v108, s30, v112, v109
	v_add_f32_e32 v108, 1.0, v108
	v_mul_f32_e32 v104, v104, v108
	v_add_f32_e32 v102, v102, v134
	v_bfi_b32 v135, s30, v123, v113
	v_mov_b32_e32 v132, v103
	v_mul_f32_e32 v104, v102, v104
	v_mul_f32_e32 v106, 0.5, v106
	v_pk_add_f32 v[102:103], v[132:133], v[134:135]
	v_bfi_b32 v135, s30, v138, v131
	v_mul_f32_e32 v103, v106, v103
	v_mul_f32_e32 v102, v102, v103
	v_mov_b32_e32 v132, v105
	v_cvt_pk_bf16_f32 v102, v104, v102
	v_mul_f32_e32 v103, 0.5, v107
	v_pk_add_f32 v[104:105], v[132:133], v[134:135]
	s_nop 0
	v_mul_f32_e32 v103, v103, v105
	v_mul_f32_e32 v103, v104, v103
	v_cvt_pk_bf16_f32 v103, v125, v103
	global_store_dwordx2 v[110:111], v[102:103], off offset:2112
	v_mov_b64_e32 v[102:103], v[180:181]
	v_lshlrev_b32_e32 v104, 16, v102
	v_mul_f32_e32 v105, 0x3d372713, v104
	v_mul_f32_e32 v105, v105, v104
	v_fma_f32 v105, v105, v104, v104
	v_mul_f32_e32 v105, 0x3f4c422a, v105
	v_add_f32_e64 v106, |v105|, |v105|
	v_mul_f32_e32 v106, 0x3fb8aa3b, v106
	v_exp_f32_e32 v106, v106
	s_nop 0
	v_add_f32_e32 v106, 1.0, v106
	v_rcp_f32_e32 v106, v106
	s_nop 0
	v_fma_f32 v106, v106, -2.0, 1.0
	v_and_b32_e32 v102, 0xffff0000, v102
	v_mul_f32_e32 v107, 0x3d372713, v102
	v_mul_f32_e32 v107, v107, v102
	v_fma_f32 v107, v107, v102, v102
	v_mul_f32_e32 v107, 0x3f4c422a, v107
	v_add_f32_e64 v108, |v107|, |v107|
	v_mul_f32_e32 v108, 0x3fb8aa3b, v108
	v_exp_f32_e32 v108, v108
	s_nop 0
	v_add_f32_e32 v108, 1.0, v108
	v_rcp_f32_e32 v108, v108
	s_nop 0
	v_fma_f32 v108, v108, -2.0, 1.0
	v_lshlrev_b32_e32 v109, 16, v103
	v_mul_f32_e32 v112, 0x3d372713, v109
	v_mul_f32_e32 v112, v112, v109
	v_fma_f32 v112, v112, v109, v109
	v_mul_f32_e32 v112, 0x3f4c422a, v112
	v_add_f32_e64 v113, |v112|, |v112|
	v_mul_f32_e32 v113, 0x3fb8aa3b, v113
	v_exp_f32_e32 v113, v113
	s_nop 0
	v_add_f32_e32 v113, 1.0, v113
	v_rcp_f32_e32 v113, v113
	s_nop 0
	v_fma_f32 v113, v113, -2.0, 1.0
	v_and_b32_e32 v103, 0xffff0000, v103
	v_mul_f32_e32 v123, 0x3d372713, v103
	v_mul_f32_e32 v123, v123, v103
	v_fma_f32 v123, v123, v103, v103
	v_mul_f32_e32 v123, 0x3f4c422a, v123
	v_add_f32_e64 v125, |v123|, |v123|
	v_mul_f32_e32 v125, 0x3fb8aa3b, v125
	v_exp_f32_e32 v125, v125
	s_nop 0
	v_add_f32_e32 v125, 1.0, v125
	v_rcp_f32_e32 v125, v125
	s_nop 0
	v_fma_f32 v125, v125, -2.0, 1.0
	v_bfi_b32 v112, s30, v113, v112
	v_mul_f32_e32 v109, 0.5, v109
	v_add_f32_e32 v112, 1.0, v112
	v_mul_f32_e32 v109, v109, v112
	v_add_f32_e32 v100, v100, v134
	v_mul_f32_e32 v109, v100, v109
	v_mul_f32_e32 v100, 0.5, v104
	v_bfi_b32 v104, s30, v106, v105
	v_add_f32_e32 v104, 1.0, v104
	v_mul_f32_e32 v100, v100, v104
	v_add_f32_e32 v98, v98, v134
	v_bfi_b32 v135, s30, v108, v107
	v_mov_b32_e32 v132, v99
	v_mul_f32_e32 v100, v98, v100
	v_mul_f32_e32 v102, 0.5, v102
	v_pk_add_f32 v[98:99], v[132:133], v[134:135]
	v_bfi_b32 v135, s30, v125, v123
	v_mul_f32_e32 v99, v102, v99
	v_mul_f32_e32 v98, v98, v99
	v_mov_b32_e32 v132, v101
	v_cvt_pk_bf16_f32 v98, v100, v98
	v_mul_f32_e32 v99, 0.5, v103
	v_pk_add_f32 v[100:101], v[132:133], v[134:135]
	v_or_b32_e32 v102, s18, v118
	v_mul_f32_e32 v99, v99, v101
	v_mul_f32_e32 v99, v100, v99
	v_mov_b64_e32 v[100:101], s[0:1]
	v_mad_u64_u32 v[100:101], s[2:3], v102, s11, v[100:101]
	v_mad_i32_i24 v101, s19, v157, v101
	v_lshl_add_u64 v[100:101], s[22:23], 1, v[100:101]
	v_lshl_add_u64 v[100:101], v[100:101], 0, v[114:115]
	v_add_co_u32_e32 v104, vcc, 0x1000, v100
	v_cvt_pk_bf16_f32 v99, v109, v99
	s_nop 0
	v_addc_co_u32_e32 v105, vcc, 0, v101, vcc
	s_waitcnt vmcnt(3)
	v_mov_b64 v[176:177], v[184:185]
	v_mov_b64 v[178:179], v[186:187]
	v_mov_b64 v[180:181], v[188:189]
	v_mov_b64 v[104:105], v[190:191]
	s_ashr_i32 s21, s20, 31
	global_store_dwordx2 v[110:111], v[98:99], off offset:2144
	v_lshl_add_u64 v[98:99], s[20:21], 0, v[116:117]
	v_lshl_add_u64 v[98:99], v[98:99], 2, s[6:7]
	v_mov_b32_e32 v98, v192
	v_mov_b32_e32 v103, s19
	v_lshlrev_b32_e32 v99, 16, v104
	v_mul_f32_e32 v106, 0x3d372713, v99
	v_mul_f32_e32 v106, v106, v99
	v_fma_f32 v106, v106, v99, v99
	v_mul_f32_e32 v106, 0x3f4c422a, v106
	v_add_f32_e64 v107, |v106|, |v106|
	v_mul_f32_e32 v107, 0x3fb8aa3b, v107
	v_exp_f32_e32 v107, v107
	s_nop 0
	v_add_f32_e32 v107, 1.0, v107
	v_rcp_f32_e32 v107, v107
	s_nop 0
	v_fma_f32 v107, v107, -2.0, 1.0
	v_and_b32_e32 v104, 0xffff0000, v104
	v_mul_f32_e32 v108, 0x3d372713, v104
	v_mul_f32_e32 v108, v108, v104
	v_fma_f32 v108, v108, v104, v104
	v_mul_f32_e32 v108, 0x3f4c422a, v108
	v_add_f32_e64 v109, |v108|, |v108|
	v_mul_f32_e32 v109, 0x3fb8aa3b, v109
	v_exp_f32_e32 v109, v109
	s_nop 0
	v_add_f32_e32 v109, 1.0, v109
	v_rcp_f32_e32 v109, v109
	s_nop 0
	v_fma_f32 v109, v109, -2.0, 1.0
	v_lshlrev_b32_e32 v110, 16, v105
	v_mul_f32_e32 v111, 0x3d372713, v110
	v_mul_f32_e32 v111, v111, v110
	v_fma_f32 v111, v111, v110, v110
	v_mul_f32_e32 v111, 0x3f4c422a, v111
	v_add_f32_e64 v112, |v111|, |v111|
	v_mul_f32_e32 v112, 0x3fb8aa3b, v112
	v_exp_f32_e32 v112, v112
	s_nop 0
	v_add_f32_e32 v112, 1.0, v112
	v_rcp_f32_e32 v112, v112
	s_nop 0
	v_fma_f32 v112, v112, -2.0, 1.0
	v_and_b32_e32 v105, 0xffff0000, v105
	v_mul_f32_e32 v113, 0x3d372713, v105
	v_mul_f32_e32 v113, v113, v105
	v_fma_f32 v113, v113, v105, v105
	v_mul_f32_e32 v113, 0x3f4c422a, v113
	v_add_f32_e64 v123, |v113|, |v113|
	v_mul_f32_e32 v123, 0x3fb8aa3b, v123
	v_exp_f32_e32 v123, v123
	s_nop 0
	v_add_f32_e32 v123, 1.0, v123
	v_rcp_f32_e32 v123, v123
	s_nop 0
	v_fma_f32 v123, v123, -2.0, 1.0
	v_bfi_b32 v111, s30, v112, v111
	v_mul_f32_e32 v110, 0.5, v110
	v_add_f32_e32 v111, 1.0, v111
	v_mul_f32_e32 v110, v110, v111
	v_add_f32_e32 v96, v96, v98
	v_mul_f32_e32 v110, v96, v110
	v_mul_f32_e32 v96, 0.5, v99
	v_bfi_b32 v99, s30, v107, v106
	v_add_f32_e32 v99, 1.0, v99
	v_mul_f32_e32 v96, v96, v99
	v_add_f32_e32 v94, v94, v98
	v_bfi_b32 v99, s30, v109, v108
	v_mov_b32_e32 v132, v95
	v_mul_f32_e32 v96, v94, v96
	v_mul_f32_e32 v104, 0.5, v104
	v_pk_add_f32 v[94:95], v[132:133], v[98:99]
	v_bfi_b32 v99, s30, v123, v113
	v_mul_f32_e32 v95, v104, v95
	v_mul_f32_e32 v94, v94, v95
	v_mov_b32_e32 v132, v97
	v_cvt_pk_bf16_f32 v96, v96, v94
	v_lshlrev_b64 v[94:95], 12, v[102:103]
	v_mul_f32_e32 v104, 0.5, v105
	v_pk_add_f32 v[102:103], v[132:133], v[98:99]
	v_lshl_add_u64 v[94:95], s[12:13], 0, v[94:95]
	v_mul_f32_e32 v97, v104, v103
	v_lshl_add_u64 v[94:95], s[22:23], 1, v[94:95]
	v_mul_f32_e32 v97, v102, v97
	v_lshl_add_u64 v[100:101], v[100:101], 0, s[14:15]
	v_lshl_add_u64 v[94:95], v[94:95], 0, v[114:115]
	v_cvt_pk_bf16_f32 v97, v110, v97
	global_store_dwordx2 v[94:95], v[96:97], off offset:2048
	v_mov_b64_e32 v[96:97], v[176:177]
	v_lshlrev_b32_e32 v99, 16, v96
	v_mul_f32_e32 v102, 0x3d372713, v99
	v_mul_f32_e32 v102, v102, v99
	v_fma_f32 v102, v102, v99, v99
	v_mul_f32_e32 v102, 0x3f4c422a, v102
	v_add_f32_e64 v103, |v102|, |v102|
	v_mul_f32_e32 v103, 0x3fb8aa3b, v103
	v_exp_f32_e32 v103, v103
	s_nop 0
	v_add_f32_e32 v103, 1.0, v103
	v_rcp_f32_e32 v103, v103
	s_nop 0
	v_fma_f32 v103, v103, -2.0, 1.0
	v_and_b32_e32 v96, 0xffff0000, v96
	v_mul_f32_e32 v104, 0x3d372713, v96
	v_mul_f32_e32 v104, v104, v96
	v_fma_f32 v104, v104, v96, v96
	v_mul_f32_e32 v104, 0x3f4c422a, v104
	v_add_f32_e64 v105, |v104|, |v104|
	v_mul_f32_e32 v105, 0x3fb8aa3b, v105
	v_exp_f32_e32 v105, v105
	s_nop 0
	v_add_f32_e32 v105, 1.0, v105
	v_rcp_f32_e32 v105, v105
	s_nop 0
	v_fma_f32 v105, v105, -2.0, 1.0
	v_lshlrev_b32_e32 v106, 16, v97
	v_mul_f32_e32 v107, 0x3d372713, v106
	v_mul_f32_e32 v107, v107, v106
	v_fma_f32 v107, v107, v106, v106
	v_mul_f32_e32 v107, 0x3f4c422a, v107
	v_add_f32_e64 v108, |v107|, |v107|
	v_mul_f32_e32 v108, 0x3fb8aa3b, v108
	v_exp_f32_e32 v108, v108
	s_nop 0
	v_add_f32_e32 v108, 1.0, v108
	v_rcp_f32_e32 v108, v108
	s_nop 0
	v_fma_f32 v108, v108, -2.0, 1.0
	v_and_b32_e32 v97, 0xffff0000, v97
	v_mul_f32_e32 v109, 0x3d372713, v97
	v_mul_f32_e32 v109, v109, v97
	v_fma_f32 v109, v109, v97, v97
	v_mul_f32_e32 v109, 0x3f4c422a, v109
	v_add_f32_e64 v110, |v109|, |v109|
	v_mul_f32_e32 v110, 0x3fb8aa3b, v110
	v_exp_f32_e32 v110, v110
	s_nop 0
	v_add_f32_e32 v110, 1.0, v110
	v_rcp_f32_e32 v110, v110
	s_nop 0
	v_fma_f32 v110, v110, -2.0, 1.0
	v_bfi_b32 v107, s30, v108, v107
	v_mul_f32_e32 v106, 0.5, v106
	v_add_f32_e32 v107, 1.0, v107
	v_mul_f32_e32 v106, v106, v107
	v_add_f32_e32 v92, v92, v98
	v_mul_f32_e32 v106, v92, v106
	v_mul_f32_e32 v92, 0.5, v99
	v_bfi_b32 v99, s30, v103, v102
	v_add_f32_e32 v99, 1.0, v99
	v_mul_f32_e32 v92, v92, v99
	v_add_f32_e32 v90, v90, v98
	v_bfi_b32 v99, s30, v105, v104
	v_mov_b32_e32 v132, v91
	v_mul_f32_e32 v92, v90, v92
	v_mul_f32_e32 v96, 0.5, v96
	v_pk_add_f32 v[90:91], v[132:133], v[98:99]
	v_bfi_b32 v99, s30, v110, v109
	v_mul_f32_e32 v91, v96, v91
	v_mul_f32_e32 v90, v90, v91
	v_mov_b32_e32 v132, v93
	v_cvt_pk_bf16_f32 v90, v92, v90
	v_mul_f32_e32 v91, 0.5, v97
	v_pk_add_f32 v[92:93], v[132:133], v[98:99]
	s_nop 0
	v_mul_f32_e32 v91, v91, v93
	v_mul_f32_e32 v91, v92, v91
	v_cvt_pk_bf16_f32 v91, v106, v91
	global_store_dwordx2 v[94:95], v[90:91], off offset:2080
	v_mov_b64_e32 v[90:91], v[178:179]
	v_lshlrev_b32_e32 v92, 16, v90
	v_mul_f32_e32 v93, 0x3d372713, v92
	v_mul_f32_e32 v93, v93, v92
	v_fma_f32 v93, v93, v92, v92
	v_mul_f32_e32 v93, 0x3f4c422a, v93
	v_add_f32_e64 v96, |v93|, |v93|
	v_mul_f32_e32 v96, 0x3fb8aa3b, v96
	v_exp_f32_e32 v96, v96
	s_nop 0
	v_add_f32_e32 v96, 1.0, v96
	v_rcp_f32_e32 v96, v96
	s_nop 0
	v_fma_f32 v96, v96, -2.0, 1.0
	v_and_b32_e32 v90, 0xffff0000, v90
	v_mul_f32_e32 v97, 0x3d372713, v90
	v_mul_f32_e32 v97, v97, v90
	v_fma_f32 v97, v97, v90, v90
	v_mul_f32_e32 v97, 0x3f4c422a, v97
	v_add_f32_e64 v99, |v97|, |v97|
	v_mul_f32_e32 v99, 0x3fb8aa3b, v99
	v_exp_f32_e32 v99, v99
	s_nop 0
	v_add_f32_e32 v99, 1.0, v99
	v_rcp_f32_e32 v99, v99
	s_nop 0
	v_fma_f32 v99, v99, -2.0, 1.0
	v_lshlrev_b32_e32 v102, 16, v91
	v_mul_f32_e32 v103, 0x3d372713, v102
	v_mul_f32_e32 v103, v103, v102
	v_fma_f32 v103, v103, v102, v102
	v_mul_f32_e32 v103, 0x3f4c422a, v103
	v_add_f32_e64 v104, |v103|, |v103|
	v_mul_f32_e32 v104, 0x3fb8aa3b, v104
	v_exp_f32_e32 v104, v104
	s_nop 0
	v_add_f32_e32 v104, 1.0, v104
	v_rcp_f32_e32 v104, v104
	s_nop 0
	v_fma_f32 v104, v104, -2.0, 1.0
	v_and_b32_e32 v91, 0xffff0000, v91
	v_mul_f32_e32 v105, 0x3d372713, v91
	v_mul_f32_e32 v105, v105, v91
	v_fma_f32 v105, v105, v91, v91
	v_mul_f32_e32 v105, 0x3f4c422a, v105
	v_add_f32_e64 v106, |v105|, |v105|
	v_mul_f32_e32 v106, 0x3fb8aa3b, v106
	v_exp_f32_e32 v106, v106
	s_nop 0
	v_add_f32_e32 v106, 1.0, v106
	v_rcp_f32_e32 v106, v106
	s_nop 0
	v_fma_f32 v106, v106, -2.0, 1.0
	v_bfi_b32 v103, s30, v104, v103
	v_mul_f32_e32 v102, 0.5, v102
	v_add_f32_e32 v103, 1.0, v103
	v_mul_f32_e32 v102, v102, v103
	v_add_f32_e32 v88, v88, v98
	v_mul_f32_e32 v102, v88, v102
	v_mul_f32_e32 v88, 0.5, v92
	v_bfi_b32 v92, s30, v96, v93
	v_add_f32_e32 v92, 1.0, v92
	v_mul_f32_e32 v88, v88, v92
	v_add_f32_e32 v86, v86, v98
	v_bfi_b32 v99, s30, v99, v97
	v_mov_b32_e32 v132, v87
	v_mul_f32_e32 v88, v86, v88
	v_mul_f32_e32 v90, 0.5, v90
	v_pk_add_f32 v[86:87], v[132:133], v[98:99]
	v_bfi_b32 v99, s30, v106, v105
	v_mul_f32_e32 v87, v90, v87
	v_mul_f32_e32 v86, v86, v87
	v_mov_b32_e32 v132, v89
	v_cvt_pk_bf16_f32 v86, v88, v86
	v_mul_f32_e32 v87, 0.5, v91
	v_pk_add_f32 v[88:89], v[132:133], v[98:99]
	s_nop 0
	v_mul_f32_e32 v87, v87, v89
	v_mul_f32_e32 v87, v88, v87
	v_cvt_pk_bf16_f32 v87, v102, v87
	global_store_dwordx2 v[94:95], v[86:87], off offset:2112
	v_mov_b64_e32 v[86:87], v[180:181]
	v_lshlrev_b32_e32 v88, 16, v86
	v_mul_f32_e32 v89, 0x3d372713, v88
	v_mul_f32_e32 v89, v89, v88
	v_fma_f32 v89, v89, v88, v88
	v_mul_f32_e32 v89, 0x3f4c422a, v89
	v_add_f32_e64 v90, |v89|, |v89|
	v_mul_f32_e32 v90, 0x3fb8aa3b, v90
	v_exp_f32_e32 v90, v90
	s_nop 0
	v_add_f32_e32 v90, 1.0, v90
	v_rcp_f32_e32 v90, v90
	s_nop 0
	v_fma_f32 v90, v90, -2.0, 1.0
	v_and_b32_e32 v86, 0xffff0000, v86
	v_mul_f32_e32 v91, 0x3d372713, v86
	v_mul_f32_e32 v91, v91, v86
	v_fma_f32 v91, v91, v86, v86
	v_mul_f32_e32 v91, 0x3f4c422a, v91
	v_add_f32_e64 v92, |v91|, |v91|
	v_mul_f32_e32 v92, 0x3fb8aa3b, v92
	v_exp_f32_e32 v92, v92
	s_nop 0
	v_add_f32_e32 v92, 1.0, v92
	v_rcp_f32_e32 v92, v92
	s_nop 0
	v_fma_f32 v92, v92, -2.0, 1.0
	v_lshlrev_b32_e32 v93, 16, v87
	v_mul_f32_e32 v96, 0x3d372713, v93
	v_mul_f32_e32 v96, v96, v93
	v_fma_f32 v96, v96, v93, v93
	v_mul_f32_e32 v96, 0x3f4c422a, v96
	v_add_f32_e64 v97, |v96|, |v96|
	v_mul_f32_e32 v97, 0x3fb8aa3b, v97
	v_exp_f32_e32 v97, v97
	s_nop 0
	v_add_f32_e32 v97, 1.0, v97
	v_rcp_f32_e32 v97, v97
	s_nop 0
	v_fma_f32 v97, v97, -2.0, 1.0
	v_and_b32_e32 v87, 0xffff0000, v87
	v_mul_f32_e32 v99, 0x3d372713, v87
	v_mul_f32_e32 v99, v99, v87
	v_fma_f32 v99, v99, v87, v87
	v_mul_f32_e32 v100, 0x3f4c422a, v99
	v_cmp_nlt_f32_e64 s[2:3], |v100|, s26
	s_and_saveexec_b64 s[18:19], s[2:3]
	s_xor_b64 s[18:19], exec, s[18:19]
	s_cbranch_execz .LBB0_3450
	v_add_f32_e64 v99, |v100|, |v100|
	v_mul_f32_e32 v101, 0x3fb8aa3b, v99
	v_rndne_f32_e32 v102, v101
	v_sub_f32_e32 v103, v101, v102
	v_fma_f32 v101, v99, s27, -v101
	v_fmac_f32_e32 v101, 0x32a5705f, v99
	v_add_f32_e32 v101, v103, v101
	v_cvt_i32_f32_e32 v102, v102
	v_exp_f32_e32 v101, v101
	v_cmp_ngt_f32_e32 vcc, s28, v99
	v_ldexp_f32 v101, v101, v102
	s_nop 0
	v_cndmask_b32_e32 v101, 0, v101, vcc
	v_cmp_nlt_f32_e32 vcc, s29, v99
	s_nop 1
	v_cndmask_b32_e32 v99, v158, v101, vcc
	v_add_f32_e32 v99, 1.0, v99
	v_rcp_f32_e32 v99, v99
	s_nop 0
	v_fma_f32 v101, v99, -2.0, 1.0
